# LN+router pass 1: LayerNorm gain/bias hoisted into 64 dead VGPRs (16 loads + four full drains per row removed); counted waits before the tail copy of the next row's raw registers and at the prefetch h
# speedup vs baseline: 1.0063x; 1.0063x over previous
.LBB0_915:
	s_lshl_b32 s34, s90, 12
	v_readlane_b32 s48, v251, 0
	s_lshl_b64 s[12:13], s[34:35], 2
	v_readlane_b32 s50, v251, 2
	v_readlane_b32 s51, v251, 3
	s_add_u32 s38, s50, s12
	v_readlane_b32 s52, v251, 4
	s_addc_u32 s39, s51, s13
	v_readlane_b32 s53, v251, 5
	s_add_u32 s12, s52, s12
	v_and_b32_e32 v136, 63, v1
	s_addc_u32 s13, s53, s13
	v_lshlrev_b32_e32 v2, 5, v136
	v_lshl_add_u64 v[138:139], s[38:39], 0, v[2:3]
	v_lshl_add_u64 v[140:141], s[12:13], 0, v[2:3]
	v_or_b32_e32 v4, 0x1000, v2
	v_mov_b32_e32 v5, v3
	v_or_b32_e32 v2, 0x1800, v2
	v_lshl_add_u64 v[144:145], s[12:13], 0, v[4:5]
	v_lshl_add_u64 v[148:149], s[12:13], 0, v[2:3]
	v_readlane_b32 s12, v254, 44
	s_lshr_b32 s13, s14, 4
	s_add_i32 s12, s12, s33
	s_and_b32 s33, s13, 12
	s_lshl_b32 s13, s15, 14
	s_add_i32 s34, s13, 0
	s_lshl_b64 s[8:9], s[8:9], 12
	s_add_u32 s8, s22, s8
	v_lshl_add_u64 v[142:143], s[38:39], 0, v[4:5]
	v_lshl_add_u64 v[146:147], s[38:39], 0, v[2:3]
	v_lshlrev_b32_e32 v2, 4, v136
	s_addc_u32 s9, s23, s9
	global_load_dwordx4 v[158:161], v[138:139], off offset:16
	global_load_dwordx4 v[162:165], v[138:139], off
	global_load_dwordx4 v[166:169], v[140:141], off offset:16
	global_load_dwordx4 v[170:173], v[140:141], off
	global_load_dwordx4 v[174:177], v[140:141], off offset:2048
	global_load_dwordx4 v[178:181], v[138:139], off offset:2048
	global_load_dwordx4 v[182:185], v[138:139], off offset:2064
	global_load_dwordx4 v[186:189], v[140:141], off offset:2064
	global_load_dwordx4 v[190:193], v[144:145], off
	global_load_dwordx4 v[194:197], v[142:143], off
	global_load_dwordx4 v[198:201], v[142:143], off offset:16
	global_load_dwordx4 v[204:207], v[144:145], off offset:16
	global_load_dwordx4 v[208:211], v[148:149], off
	global_load_dwordx4 v[212:215], v[146:147], off
	global_load_dwordx4 v[216:219], v[146:147], off offset:16
	global_load_dwordx4 v[220:223], v[148:149], off offset:16
	s_waitcnt vmcnt(0)
	v_mov_b64_e32 v[64:65], v[132:133]
	v_mov_b64_e32 v[48:49], v[128:129]
	v_mov_b64_e32 v[32:33], v[124:125]
	v_mov_b64_e32 v[16:17], v[120:121]
	v_mov_b64_e32 v[8:9], v[116:117]
	v_mov_b64_e32 v[12:13], v[100:101]
	v_mov_b64_e32 v[24:25], v[112:113]
	v_mov_b64_e32 v[28:29], v[96:97]
	v_mov_b64_e32 v[40:41], v[108:109]
	v_mov_b64_e32 v[44:45], v[92:93]
	v_mov_b64_e32 v[56:57], v[104:105]
	v_mov_b64_e32 v[60:61], v[88:89]
	v_mov_b64_e32 v[4:5], v[68:69]
	v_mov_b64_e32 v[20:21], v[72:73]
	v_mov_b64_e32 v[36:37], v[80:81]
	v_mov_b64_e32 v[52:53], v[76:77]
	v_or_b32_e32 v154, 64, v136
	v_or_b32_e32 v155, 0x80, v136
	v_or_b32_e32 v156, 0xc0, v136
	v_lshl_add_u64 v[150:151], s[8:9], 0, v[2:3]
	s_mov_b32 s38, 0
	v_mov_b64_e32 v[66:67], v[134:135]
	v_mov_b64_e32 v[50:51], v[130:131]
	v_mov_b64_e32 v[34:35], v[126:127]
	v_mov_b64_e32 v[18:19], v[122:123]
	v_mov_b64_e32 v[10:11], v[118:119]
	v_mov_b64_e32 v[14:15], v[102:103]
	v_mov_b64_e32 v[26:27], v[114:115]
	v_mov_b64_e32 v[30:31], v[98:99]
	v_mov_b64_e32 v[42:43], v[110:111]
	v_mov_b64_e32 v[46:47], v[94:95]
	v_mov_b64_e32 v[58:59], v[106:107]
	v_mov_b64_e32 v[62:63], v[90:91]
	v_mov_b64_e32 v[6:7], v[70:71]
	v_mov_b64_e32 v[22:23], v[74:75]
	v_mov_b64_e32 v[38:39], v[82:83]
	v_mov_b64_e32 v[54:55], v[78:79]
	v_readlane_b32 s49, v251, 1
	v_readlane_b32 s54, v251, 6
	v_readlane_b32 s55, v251, 7
	s_branch .LBB0_917
.LBB0_916:
	v_lshlrev_b32_e32 v152, 16, v120
	v_and_b32_e32 v120, 0xffff0000, v120
	v_lshlrev_b32_e32 v153, 16, v121
	v_and_b32_e32 v121, 0xffff0000, v121
	v_cndmask_b32_e64 v117, v117, v120, s[4:5]
	v_cndmask_b32_e64 v119, v119, v121, s[4:5]
	v_lshlrev_b32_e32 v120, 16, v122
	v_and_b32_e32 v121, 0xffff0000, v122
	v_lshlrev_b32_e32 v122, 16, v123
	v_and_b32_e32 v123, 0xffff0000, v123
	v_cndmask_b32_e64 v116, v116, v152, s[4:5]
	v_cndmask_b32_e64 v118, v118, v153, s[4:5]
	v_cndmask_b32_e64 v101, v101, v121, s[4:5]
	v_cndmask_b32_e64 v100, v100, v120, s[4:5]
	v_cndmask_b32_e64 v121, v103, v123, s[4:5]
	v_cndmask_b32_e64 v120, v102, v122, s[4:5]
	v_lshlrev_b32_e32 v122, 16, v68
	v_and_b32_e32 v123, 0xffff0000, v68
	v_lshlrev_b32_e32 v68, 16, v69
	v_and_b32_e32 v69, 0xffff0000, v69
	v_pk_fma_f32 v[102:103], v[118:119], s[28:29], v[68:69] op_sel_hi:[1,0,1]
	v_pk_fma_f32 v[118:119], v[116:117], s[28:29], v[122:123] op_sel_hi:[1,0,1]
	v_lshlrev_b32_e32 v68, 16, v70
	v_and_b32_e32 v69, 0xffff0000, v70
	v_lshlrev_b32_e32 v70, 16, v71
	v_and_b32_e32 v71, 0xffff0000, v71
	v_pk_fma_f32 v[116:117], v[120:121], s[28:29], v[70:71] op_sel_hi:[1,0,1]
	v_pk_fma_f32 v[120:121], v[100:101], s[28:29], v[68:69] op_sel_hi:[1,0,1]
	v_add_f32_e32 v68, v118, v119
	v_add_f32_e32 v69, v102, v103
	v_add_f32_e32 v68, v68, v69
	v_add_f32_e32 v69, v120, v121
	v_add_f32_e32 v70, v116, v117
	v_add_f32_e32 v69, v69, v70
	v_add_f32_e32 v68, v69, v68
	v_add_f32_e32 v122, 0, v68
	v_lshlrev_b32_e32 v68, 16, v124
	v_and_b32_e32 v69, 0xffff0000, v124
	v_lshlrev_b32_e32 v70, 16, v125
	v_and_b32_e32 v71, 0xffff0000, v125
	v_lshlrev_b32_e32 v100, 16, v126
	v_and_b32_e32 v101, 0xffff0000, v126
	v_cndmask_b32_e64 v69, v113, v69, s[4:5]
	v_cndmask_b32_e64 v68, v112, v68, s[4:5]
	v_cndmask_b32_e64 v71, v115, v71, s[4:5]
	v_cndmask_b32_e64 v70, v114, v70, s[4:5]
	v_lshlrev_b32_e32 v114, 16, v127
	v_and_b32_e32 v115, 0xffff0000, v127
	v_cndmask_b32_e64 v113, v97, v101, s[4:5]
	v_cndmask_b32_e64 v112, v96, v100, s[4:5]
	v_lshlrev_b32_e32 v100, 16, v72
	v_and_b32_e32 v101, 0xffff0000, v72
	v_lshlrev_b32_e32 v72, 16, v73
	v_and_b32_e32 v73, 0xffff0000, v73
	v_cndmask_b32_e64 v99, v99, v115, s[4:5]
	v_cndmask_b32_e64 v98, v98, v114, s[4:5]
	v_pk_fma_f32 v[96:97], v[70:71], s[28:29], v[72:73] op_sel_hi:[1,0,1]
	v_pk_fma_f32 v[100:101], v[68:69], s[28:29], v[100:101] op_sel_hi:[1,0,1]
	v_lshlrev_b32_e32 v68, 16, v74
	v_and_b32_e32 v69, 0xffff0000, v74
	v_lshlrev_b32_e32 v70, 16, v75
	v_and_b32_e32 v71, 0xffff0000, v75
	v_pk_fma_f32 v[98:99], v[98:99], s[28:29], v[70:71] op_sel_hi:[1,0,1]
	v_pk_fma_f32 v[112:113], v[112:113], s[28:29], v[68:69] op_sel_hi:[1,0,1]
	v_add_f32_e32 v68, v100, v101
	v_add_f32_e32 v69, v96, v97
	v_add_f32_e32 v68, v68, v69
	v_add_f32_e32 v69, v112, v113
	v_add_f32_e32 v70, v98, v99
	v_add_f32_e32 v69, v69, v70
	v_add_f32_e32 v68, v69, v68
	v_add_f32_e32 v114, v122, v68
	v_lshlrev_b32_e32 v68, 16, v128
	v_and_b32_e32 v69, 0xffff0000, v128
	v_lshlrev_b32_e32 v70, 16, v129
	v_and_b32_e32 v71, 0xffff0000, v129
	v_lshlrev_b32_e32 v72, 16, v130
	v_and_b32_e32 v73, 0xffff0000, v130
	v_cndmask_b32_e64 v69, v109, v69, s[4:5]
	v_cndmask_b32_e64 v68, v108, v68, s[4:5]
	v_cndmask_b32_e64 v71, v111, v71, s[4:5]
	v_cndmask_b32_e64 v70, v110, v70, s[4:5]
	v_lshlrev_b32_e32 v74, 16, v131
	v_and_b32_e32 v75, 0xffff0000, v131
	v_cndmask_b32_e64 v73, v93, v73, s[4:5]
	v_cndmask_b32_e64 v72, v92, v72, s[4:5]
	v_lshlrev_b32_e32 v92, 16, v80
	v_and_b32_e32 v93, 0xffff0000, v80
	v_lshlrev_b32_e32 v80, 16, v81
	v_and_b32_e32 v81, 0xffff0000, v81
	v_cndmask_b32_e64 v75, v95, v75, s[4:5]
	v_cndmask_b32_e64 v74, v94, v74, s[4:5]
	v_pk_fma_f32 v[80:81], v[70:71], s[28:29], v[80:81] op_sel_hi:[1,0,1]
	v_pk_fma_f32 v[92:93], v[68:69], s[28:29], v[92:93] op_sel_hi:[1,0,1]
	v_lshlrev_b32_e32 v68, 16, v82
	v_and_b32_e32 v69, 0xffff0000, v82
	v_lshlrev_b32_e32 v70, 16, v83
	v_and_b32_e32 v71, 0xffff0000, v83
	v_pk_fma_f32 v[82:83], v[74:75], s[28:29], v[70:71] op_sel_hi:[1,0,1]
	v_pk_fma_f32 v[94:95], v[72:73], s[28:29], v[68:69] op_sel_hi:[1,0,1]
	v_add_f32_e32 v68, v92, v93
	v_add_f32_e32 v69, v80, v81
	v_add_f32_e32 v68, v68, v69
	v_add_f32_e32 v69, v94, v95
	v_add_f32_e32 v70, v82, v83
	v_add_f32_e32 v69, v69, v70
	v_add_f32_e32 v68, v69, v68
	v_add_f32_e32 v108, v114, v68
	v_lshlrev_b32_e32 v68, 16, v132
	v_and_b32_e32 v69, 0xffff0000, v132
	v_lshlrev_b32_e32 v72, 16, v133
	v_and_b32_e32 v73, 0xffff0000, v133
	v_cndmask_b32_e64 v71, v105, v69, s[4:5]
	v_cndmask_b32_e64 v70, v104, v68, s[4:5]
	v_cndmask_b32_e64 v69, v107, v73, s[4:5]
	v_cndmask_b32_e64 v68, v106, v72, s[4:5]
	v_lshlrev_b32_e32 v72, 16, v134
	v_and_b32_e32 v73, 0xffff0000, v134
	v_lshlrev_b32_e32 v104, 16, v135
	v_and_b32_e32 v105, 0xffff0000, v135
	v_cndmask_b32_e64 v75, v89, v73, s[4:5]
	v_cndmask_b32_e64 v74, v88, v72, s[4:5]
	v_lshlrev_b32_e32 v72, 16, v76
	v_and_b32_e32 v73, 0xffff0000, v76
	v_lshlrev_b32_e32 v76, 16, v77
	v_and_b32_e32 v77, 0xffff0000, v77
	v_cndmask_b32_e64 v89, v91, v105, s[4:5]
	v_cndmask_b32_e64 v88, v90, v104, s[4:5]
	v_pk_fma_f32 v[68:69], v[68:69], s[28:29], v[76:77] op_sel_hi:[1,0,1]
	v_pk_fma_f32 v[72:73], v[70:71], s[28:29], v[72:73] op_sel_hi:[1,0,1]
	v_lshlrev_b32_e32 v76, 16, v78
	v_and_b32_e32 v77, 0xffff0000, v78
	v_lshlrev_b32_e32 v70, 16, v79
	v_and_b32_e32 v71, 0xffff0000, v79
	v_pk_fma_f32 v[70:71], v[88:89], s[28:29], v[70:71] op_sel_hi:[1,0,1]
	v_pk_fma_f32 v[74:75], v[74:75], s[28:29], v[76:77] op_sel_hi:[1,0,1]
	v_add_f32_e32 v76, v72, v73
	v_add_f32_e32 v77, v68, v69
	v_add_f32_e32 v76, v76, v77
	v_add_f32_e32 v77, v74, v75
	v_add_f32_e32 v78, v70, v71
	v_add_f32_e32 v77, v77, v78
	v_add_f32_e32 v76, v77, v76
	v_and_b32_e32 v77, 64, v229
	v_add_u32_e32 v77, 64, v77
	v_xor_b32_e32 v78, 1, v229
	v_cmp_lt_i32_e32 vcc, v78, v77
	v_add_f32_e32 v76, v108, v76
	s_mov_b32 s8, 0xf800000
	v_cndmask_b32_e32 v78, v229, v78, vcc
	v_lshlrev_b32_e32 v128, 2, v78
	ds_bpermute_b32 v78, v128, v76
	s_add_i32 s12, s12, 1
	s_waitcnt lgkmcnt(0)
	v_add_f32_e32 v76, v76, v78
	v_xor_b32_e32 v78, 2, v229
	v_cmp_lt_i32_e32 vcc, v78, v77
	s_nop 1
	v_cndmask_b32_e32 v78, v229, v78, vcc
	v_lshlrev_b32_e32 v129, 2, v78
	ds_bpermute_b32 v78, v129, v76
	s_waitcnt lgkmcnt(0)
	v_add_f32_e32 v76, v76, v78
	v_xor_b32_e32 v78, 4, v229
	v_cmp_lt_i32_e32 vcc, v78, v77
	s_nop 1
	v_cndmask_b32_e32 v78, v229, v78, vcc
	v_lshlrev_b32_e32 v130, 2, v78
	ds_bpermute_b32 v78, v130, v76
	s_waitcnt lgkmcnt(0)
	v_add_f32_e32 v76, v76, v78
	v_xor_b32_e32 v78, 8, v229
	v_cmp_lt_i32_e32 vcc, v78, v77
	s_nop 1
	v_cndmask_b32_e32 v78, v229, v78, vcc
	v_lshlrev_b32_e32 v131, 2, v78
	ds_bpermute_b32 v78, v131, v76
	s_waitcnt lgkmcnt(0)
	v_add_f32_e32 v76, v76, v78
	v_xor_b32_e32 v78, 16, v229
	v_cmp_lt_i32_e32 vcc, v78, v77
	s_nop 1
	v_cndmask_b32_e32 v78, v229, v78, vcc
	v_lshlrev_b32_e32 v132, 2, v78
	ds_bpermute_b32 v78, v132, v76
	s_waitcnt lgkmcnt(0)
	v_add_f32_e32 v76, v76, v78
	v_xor_b32_e32 v78, 32, v229
	v_cmp_lt_i32_e32 vcc, v78, v77
	s_nop 1
	v_cndmask_b32_e32 v77, v229, v78, vcc
	v_lshlrev_b32_e32 v133, 2, v77
	ds_bpermute_b32 v77, v133, v76
	s_waitcnt lgkmcnt(0)
	v_add_f32_e32 v104, v76, v77
	v_fmamk_f32 v119, v104, 0xba000000, v119
	v_fmamk_f32 v121, v104, 0xba000000, v121
	v_fmamk_f32 v103, v104, 0xba000000, v103
	v_fmac_f32_e32 v118, 0xba000000, v104
	v_fmamk_f32 v117, v104, 0xba000000, v117
	v_fmac_f32_e32 v120, 0xba000000, v104
	v_mov_b32_e32 v78, v119
	v_mov_b32_e32 v79, v121
	v_fmac_f32_e32 v102, 0xba000000, v104
	v_fmac_f32_e32 v116, 0xba000000, v104
	v_mov_b32_e32 v76, v118
	v_mov_b32_e32 v77, v120
	v_pk_mul_f32 v[78:79], v[78:79], v[78:79]
	v_mov_b32_e32 v88, v103
	v_mov_b32_e32 v89, v117
	v_pk_fma_f32 v[76:77], v[76:77], v[76:77], v[78:79]
	v_mov_b32_e32 v78, v102
	v_mov_b32_e32 v79, v116
	v_pk_mul_f32 v[88:89], v[88:89], v[88:89]
	v_fmamk_f32 v101, v104, 0xba000000, v101
	v_pk_fma_f32 v[78:79], v[78:79], v[78:79], v[88:89]
	v_fmac_f32_e32 v100, 0xba000000, v104
	v_pk_add_f32 v[76:77], v[76:77], v[78:79]
	v_fmamk_f32 v97, v104, 0xba000000, v97
	v_fmac_f32_e32 v96, 0xba000000, v104
	v_pk_add_f32 v[76:77], v[76:77], v[76:77] op_sel_hi:[0,1]
	v_pk_mul_f32 v[78:79], v[96:97], v[96:97]
	v_pk_mul_f32 v[88:89], v[100:101], v[100:101]
	v_fmac_f32_e32 v112, 0xba000000, v104
	v_pk_mov_b32 v[90:91], v[88:89], v[78:79] op_sel:[1,0]
	v_mov_b32_e32 v89, v79
	v_fmamk_f32 v113, v104, 0xba000000, v113
	v_fmac_f32_e32 v98, 0xba000000, v104
	v_mul_f32_e32 v76, v112, v112
	v_pk_add_f32 v[78:79], v[90:91], v[88:89]
	v_fmamk_f32 v99, v104, 0xba000000, v99
	v_pk_fma_f32 v[88:89], v[112:113], v[112:113], v[76:77] op_sel_hi:[1,1,0]
	v_mul_f32_e32 v76, v98, v98
	v_pk_add_f32 v[78:79], v[78:79], v[78:79] op_sel_hi:[0,1]
	v_pk_fma_f32 v[90:91], v[98:99], v[98:99], v[76:77] op_sel_hi:[1,1,0]
	v_fmamk_f32 v81, v104, 0xba000000, v81
	v_fmac_f32_e32 v80, 0xba000000, v104
	v_fmamk_f32 v93, v104, 0xba000000, v93
	v_fmac_f32_e32 v92, 0xba000000, v104
	v_mul_f32_e32 v88, v92, v92
	v_mul_f32_e32 v90, v93, v93
	v_mul_f32_e32 v78, v80, v80
	v_mul_f32_e32 v76, v81, v81
	v_pk_add_f32 v[88:89], v[88:89], v[90:91]
	v_pk_add_f32 v[76:77], v[78:79], v[76:77]
	v_fmamk_f32 v95, v104, 0xba000000, v95
	v_fmac_f32_e32 v94, 0xba000000, v104
	v_fmamk_f32 v83, v104, 0xba000000, v83
	v_fmac_f32_e32 v82, 0xba000000, v104
	v_pk_add_f32 v[76:77], v[88:89], v[76:77]
	v_pk_mul_f32 v[78:79], v[82:83], v[82:83]
	v_pk_mul_f32 v[88:89], v[94:95], v[94:95]
	v_fmamk_f32 v73, v104, 0xba000000, v73
	v_pk_mov_b32 v[90:91], v[88:89], v[78:79] op_sel:[1,0]
	v_mov_b32_e32 v89, v79
	v_pk_add_f32 v[78:79], v[90:91], v[88:89]
	v_fmac_f32_e32 v72, 0xba000000, v104
	v_fmamk_f32 v69, v104, 0xba000000, v69
	v_fmac_f32_e32 v68, 0xba000000, v104
	v_fmamk_f32 v71, v104, 0xba000000, v71
	v_fmac_f32_e32 v70, 0xba000000, v104
	v_fmamk_f32 v75, v104, 0xba000000, v75
	v_fmac_f32_e32 v74, 0xba000000, v104
	v_pk_add_f32 v[76:77], v[76:77], v[76:77] op_sel_hi:[0,1]
	v_mul_f32_e32 v76, v72, v72
	v_pk_fma_f32 v[114:115], v[72:73], v[72:73], v[76:77] op_sel_hi:[1,1,0]
	v_mul_f32_e32 v76, v68, v68
	v_pk_add_f32 v[78:79], v[78:79], v[78:79] op_sel_hi:[0,1]
	v_pk_fma_f32 v[126:127], v[68:69], v[68:69], v[76:77] op_sel_hi:[1,1,0]
	v_mul_f32_e32 v114, v74, v74
	v_mul_f32_e32 v126, v75, v75
	v_mul_f32_e32 v78, v70, v70
	v_mul_f32_e32 v76, v71, v71
	v_pk_add_f32 v[114:115], v[114:115], v[126:127]
	v_pk_add_f32 v[76:77], v[78:79], v[76:77]
	s_nop 0
	v_pk_add_f32 v[76:77], v[114:115], v[76:77]
	s_nop 0
	v_add_f32_e32 v76, v76, v77
	ds_bpermute_b32 v77, v128, v76
	s_waitcnt lgkmcnt(0)
	v_add_f32_e32 v76, v76, v77
	ds_bpermute_b32 v77, v129, v76
	s_waitcnt lgkmcnt(0)
	v_add_f32_e32 v76, v76, v77
	ds_bpermute_b32 v77, v130, v76
	s_waitcnt lgkmcnt(0)
	v_add_f32_e32 v76, v76, v77
	ds_bpermute_b32 v77, v131, v76
	s_waitcnt lgkmcnt(0)
	v_add_f32_e32 v76, v76, v77
	ds_bpermute_b32 v77, v132, v76
	s_waitcnt lgkmcnt(0)
	v_add_f32_e32 v76, v76, v77
	ds_bpermute_b32 v77, v133, v76
	s_waitcnt lgkmcnt(0)
	v_add_f32_e32 v76, v76, v77
	v_fmamk_f32 v76, v76, 0x3a000000, v232
	v_mul_f32_e32 v77, 0x4f800000, v76
	v_cmp_gt_f32_e32 vcc, s8, v76
	s_nop 1
	v_cndmask_b32_e32 v76, v76, v77, vcc
	v_sqrt_f32_e32 v77, v76
	s_nop 0
	v_add_u32_e32 v78, -1, v77
	v_fma_f32 v79, -v78, v77, v76
	v_cmp_ge_f32_e64 s[8:9], 0, v79
	v_add_u32_e32 v79, 1, v77
	s_nop 0
	v_cndmask_b32_e64 v78, v77, v78, s[8:9]
	v_fma_f32 v77, -v79, v77, v76
	v_cmp_lt_f32_e64 s[8:9], 0, v77
	s_nop 1
	v_cndmask_b32_e64 v77, v78, v79, s[8:9]
	v_mul_f32_e32 v78, 0x37800000, v77
	v_cndmask_b32_e32 v77, v77, v78, vcc
	v_cmp_class_f32_e32 vcc, v76, v231
	s_nop 1
	v_cndmask_b32_e32 v76, v77, v76, vcc
	v_div_scale_f32 v77, s[8:9], v76, v76, 1.0
	v_rcp_f32_e32 v78, v77
	s_add_i32 s8, s38, s34
	s_addk_i32 s38, 0x1000
	v_fma_f32 v79, -v77, v78, 1.0
	v_fmac_f32_e32 v78, v79, v78
	v_div_scale_f32 v79, vcc, 1.0, v76, 1.0
	v_mul_f32_e32 v114, v79, v78
	v_fma_f32 v115, -v77, v114, v79
	v_fmac_f32_e32 v114, v115, v78
	v_fma_f32 v77, -v77, v114, v79
	v_div_fmas_f32 v77, v77, v78, v114
	v_div_fixup_f32 v76, v77, v76, 1.0
	v_pk_mul_f32 v[78:79], v[118:119], v[76:77] op_sel_hi:[1,0]
	v_pk_mul_f32 v[102:103], v[102:103], v[76:77] op_sel_hi:[1,0]
	v_pk_fma_f32 v[122:123], v[162:163], v[78:79], v[170:171]
	v_pk_fma_f32 v[124:125], v[164:165], v[102:103], v[172:173]
	v_pk_mul_f32 v[78:79], v[120:121], v[76:77] op_sel_hi:[1,0]
	v_pk_mul_f32 v[102:103], v[116:117], v[76:77] op_sel_hi:[1,0]
	v_pk_fma_f32 v[128:129], v[158:159], v[78:79], v[166:167]
	v_pk_fma_f32 v[126:127], v[160:161], v[102:103], v[168:169]
	v_cvt_pk_bf16_f32 v88, v122, v123
	v_cvt_pk_bf16_f32 v89, v124, v125
	v_cvt_pk_bf16_f32 v90, v128, v129
	v_cvt_pk_bf16_f32 v91, v126, v127
	global_store_dwordx4 v[150:151], v[88:91], off
	v_pk_mul_f32 v[78:79], v[100:101], v[76:77] op_sel_hi:[1,0]
	v_pk_mul_f32 v[96:97], v[96:97], v[76:77] op_sel_hi:[1,0]
	v_pk_mul_f32 v[80:81], v[80:81], v[76:77] op_sel_hi:[1,0]
	v_pk_fma_f32 v[130:131], v[180:181], v[96:97], v[176:177]
	v_pk_fma_f32 v[132:133], v[178:179], v[78:79], v[174:175]
	v_pk_mul_f32 v[78:79], v[112:113], v[76:77] op_sel_hi:[1,0]
	v_pk_mul_f32 v[96:97], v[98:99], v[76:77] op_sel_hi:[1,0]
	v_pk_fma_f32 v[118:119], v[182:183], v[78:79], v[186:187]
	v_pk_fma_f32 v[116:117], v[184:185], v[96:97], v[188:189]
	v_cvt_pk_bf16_f32 v96, v132, v133
	v_cvt_pk_bf16_f32 v97, v130, v131
	v_cvt_pk_bf16_f32 v98, v118, v119
	v_cvt_pk_bf16_f32 v99, v116, v117
	global_store_dwordx4 v[150:151], v[96:99], off offset:1024
	v_pk_mul_f32 v[78:79], v[92:93], v[76:77] op_sel_hi:[1,0]
	v_pk_fma_f32 v[120:121], v[196:197], v[80:81], v[192:193]
	v_pk_fma_f32 v[134:135], v[194:195], v[78:79], v[190:191]
	v_pk_mul_f32 v[78:79], v[94:95], v[76:77] op_sel_hi:[1,0]
	v_pk_mul_f32 v[80:81], v[82:83], v[76:77] op_sel_hi:[1,0]
	v_pk_fma_f32 v[112:113], v[198:199], v[78:79], v[204:205]
	v_pk_fma_f32 v[82:83], v[200:201], v[80:81], v[206:207]
	v_cvt_pk_bf16_f32 v78, v134, v135
	v_cvt_pk_bf16_f32 v79, v120, v121
	v_cvt_pk_bf16_f32 v80, v112, v113
	v_cvt_pk_bf16_f32 v81, v82, v83
	global_store_dwordx4 v[150:151], v[78:81], off offset:2048
	v_lshlrev_b32_e32 v77, 16, v88
	v_and_b32_e32 v88, 0xffff0000, v88
	v_lshlrev_b32_e32 v114, 16, v89
	v_and_b32_e32 v89, 0xffff0000, v89
	v_sub_f32_e32 v88, v123, v88
	v_sub_f32_e32 v77, v122, v77
	v_lshlrev_b32_e32 v115, 16, v90
	v_and_b32_e32 v90, 0xffff0000, v90
	v_lshlrev_b32_e32 v122, 16, v91
	v_and_b32_e32 v91, 0xffff0000, v91
	v_sub_f32_e32 v89, v125, v89
	v_sub_f32_e32 v114, v124, v114
	v_sub_f32_e32 v91, v127, v91
	v_sub_f32_e32 v122, v126, v122
	v_sub_f32_e32 v90, v129, v90
	v_sub_f32_e32 v115, v128, v115
	v_cvt_pk_bf16_f32 v88, v77, v88
	v_xor_b32_e32 v77, s33, v136
	v_cvt_pk_bf16_f32 v89, v114, v89
	v_cvt_pk_bf16_f32 v90, v115, v90
	v_cvt_pk_bf16_f32 v91, v122, v91
	v_lshl_add_u32 v77, v77, 4, s8
	ds_write_b128 v77, v[88:91]
	v_lshlrev_b32_e32 v77, 16, v96
	v_and_b32_e32 v88, 0xffff0000, v96
	v_lshlrev_b32_e32 v89, 16, v97
	v_and_b32_e32 v90, 0xffff0000, v97
	v_sub_f32_e32 v88, v133, v88
	v_sub_f32_e32 v77, v132, v77
	v_lshlrev_b32_e32 v91, 16, v98
	v_and_b32_e32 v96, 0xffff0000, v98
	v_lshlrev_b32_e32 v97, 16, v99
	v_and_b32_e32 v98, 0xffff0000, v99
	v_sub_f32_e32 v90, v131, v90
	v_sub_f32_e32 v89, v130, v89
	v_sub_f32_e32 v98, v117, v98
	v_sub_f32_e32 v97, v116, v97
	v_sub_f32_e32 v96, v119, v96
	v_sub_f32_e32 v91, v118, v91
	v_cvt_pk_bf16_f32 v88, v77, v88
	v_xor_b32_e32 v77, s33, v154
	v_cvt_pk_bf16_f32 v89, v89, v90
	v_cvt_pk_bf16_f32 v90, v91, v96
	v_cvt_pk_bf16_f32 v91, v97, v98
	v_lshl_add_u32 v77, v77, 4, s8
	ds_write_b128 v77, v[88:91]
	v_lshlrev_b32_e32 v77, 16, v78
	v_and_b32_e32 v78, 0xffff0000, v78
	v_sub_f32_e32 v78, v135, v78
	v_sub_f32_e32 v77, v134, v77
	v_lshlrev_b32_e32 v88, 16, v79
	v_and_b32_e32 v79, 0xffff0000, v79
	v_lshlrev_b32_e32 v89, 16, v80
	v_and_b32_e32 v80, 0xffff0000, v80
	v_lshlrev_b32_e32 v90, 16, v81
	v_and_b32_e32 v81, 0xffff0000, v81
	v_cvt_pk_bf16_f32 v78, v77, v78
	v_xor_b32_e32 v77, s33, v155
	v_sub_f32_e32 v79, v121, v79
	v_sub_f32_e32 v88, v120, v88
	v_sub_f32_e32 v81, v83, v81
	v_sub_f32_e32 v82, v82, v90
	v_sub_f32_e32 v80, v113, v80
	v_sub_f32_e32 v83, v112, v89
	v_lshl_add_u32 v77, v77, 4, s8
	v_cvt_pk_bf16_f32 v79, v88, v79
	v_cvt_pk_bf16_f32 v80, v83, v80
	v_cvt_pk_bf16_f32 v81, v82, v81
	v_pk_mul_f32 v[68:69], v[68:69], v[76:77] op_sel_hi:[1,0]
	ds_write_b128 v77, v[78:81]
	v_pk_mul_f32 v[72:73], v[72:73], v[76:77] op_sel_hi:[1,0]
	v_pk_mul_f32 v[70:71], v[70:71], v[76:77] op_sel_hi:[1,0]
	s_waitcnt vmcnt(3)
	v_mov_b64_e32 v[90:91], v[62:63]
	v_mov_b64_e32 v[98:99], v[30:31]
	v_mov_b64_e32 v[114:115], v[26:27]
	v_mov_b64_e32 v[118:119], v[10:11]
	v_mov_b64_e32 v[122:123], v[18:19]
	v_pk_fma_f32 v[78:79], v[214:215], v[68:69], v[210:211]
	v_pk_mul_f32 v[68:69], v[74:75], v[76:77] op_sel_hi:[1,0]
	v_pk_fma_f32 v[72:73], v[212:213], v[72:73], v[208:209]
	v_pk_fma_f32 v[74:75], v[218:219], v[70:71], v[222:223]
	v_pk_fma_f32 v[76:77], v[216:217], v[68:69], v[220:221]
	v_cvt_pk_bf16_f32 v68, v72, v73
	v_cvt_pk_bf16_f32 v69, v78, v79
	v_cvt_pk_bf16_f32 v70, v76, v77
	v_cvt_pk_bf16_f32 v71, v74, v75
	global_store_dwordx4 v[150:151], v[68:71], off offset:3072
	v_lshlrev_b32_e32 v80, 16, v68
	v_lshlrev_b32_e32 v81, 16, v69
	v_and_b32_e32 v68, 0xffff0000, v68
	v_and_b32_e32 v69, 0xffff0000, v69
	v_sub_f32_e32 v69, v79, v69
	v_sub_f32_e32 v68, v73, v68
	v_sub_f32_e32 v72, v72, v80
	v_lshlrev_b32_e32 v73, 16, v70
	v_and_b32_e32 v70, 0xffff0000, v70
	v_lshlrev_b32_e32 v79, 16, v71
	v_and_b32_e32 v71, 0xffff0000, v71
	v_sub_f32_e32 v78, v78, v81
	v_sub_f32_e32 v71, v75, v71
	v_sub_f32_e32 v74, v74, v79
	v_sub_f32_e32 v70, v77, v70
	v_sub_f32_e32 v73, v76, v73
	v_cvt_pk_bf16_f32 v68, v72, v68
	v_xor_b32_e32 v72, s33, v156
	v_cvt_pk_bf16_f32 v69, v78, v69
	v_cvt_pk_bf16_f32 v70, v73, v70
	v_cvt_pk_bf16_f32 v71, v74, v71
	v_lshl_add_u32 v72, v72, 4, s8
	ds_write_b128 v72, v[68:71]
	s_add_i32 s33, s33, 1
	s_mov_b64 s[8:9], 0x1000
	v_mov_b64_e32 v[78:79], v[54:55]
	v_mov_b64_e32 v[82:83], v[38:39]
	v_mov_b64_e32 v[74:75], v[22:23]
	v_mov_b64_e32 v[70:71], v[6:7]
	v_mov_b64_e32 v[106:107], v[58:59]
	v_mov_b64_e32 v[94:95], v[46:47]
	v_mov_b64_e32 v[110:111], v[42:43]
	v_mov_b64_e32 v[102:103], v[14:15]
	v_mov_b64_e32 v[126:127], v[34:35]
	v_mov_b64_e32 v[130:131], v[50:51]
	v_mov_b64_e32 v[134:135], v[66:67]
	v_lshl_add_u64 v[150:151], v[150:151], 0, s[8:9]
	s_cmpk_eq_i32 s38, 0x4000
	v_mov_b64_e32 v[76:77], v[52:53]
	v_mov_b64_e32 v[80:81], v[36:37]
	v_mov_b64_e32 v[72:73], v[20:21]
	v_mov_b64_e32 v[68:69], v[4:5]
	v_mov_b64_e32 v[88:89], v[60:61]
	v_mov_b64_e32 v[104:105], v[56:57]
	v_mov_b64_e32 v[92:93], v[44:45]
	v_mov_b64_e32 v[108:109], v[40:41]
	v_mov_b64_e32 v[96:97], v[28:29]
	v_mov_b64_e32 v[112:113], v[24:25]
	v_mov_b64_e32 v[100:101], v[12:13]
	v_mov_b64_e32 v[116:117], v[8:9]
	v_mov_b64_e32 v[120:121], v[16:17]
	v_mov_b64_e32 v[124:125], v[32:33]
	v_mov_b64_e32 v[128:129], v[48:49]
	v_mov_b64_e32 v[132:133], v[64:65]
	s_cbranch_scc1 .LBB0_934
.LBB0_917:
	s_waitcnt vmcnt(4)
	s_cmpk_lg_i32 s38, 0x3000
	s_cbranch_scc0 .LBB0_916
	v_mov_b32_e32 v4, v0
	s_ashr_i32 s13, s12, 31
	v_lshlrev_b32_e32 v4, 3, v4
	s_lshl_b64 s[8:9], s[12:13], 11
	v_and_b32_e32 v4, 0x1f8, v4
	v_or_b32_e32 v152, s8, v4
	v_mov_b32_e32 v153, s9
	v_lshl_add_u64 v[4:5], v[152:153], 1, s[40:41]
	global_load_dwordx4 v[4:7], v[4:5], off nt
	s_mov_b64 s[8:9], -1
	s_and_b64 vcc, exec, s[6:7]
	v_lshl_add_u64 v[32:33], v[152:153], 2, s[10:11]
	s_cbranch_vccnz .LBB0_920
	global_load_dwordx4 v[12:15], v[32:33], off offset:16 nt
	global_load_dwordx4 v[8:11], v[32:33], off nt
	s_mov_b64 s[8:9], 0
